# gather static priority raise given to waves 0-3 instead of waves 4-7
# speedup vs baseline: 1.0031x; 1.0031x over previous
; __device__ __forceinline__ int fresh_lane() { unsigned z = 0u; asm volatile("" : "+v"(z)); return (int)__builtin_amdgcn_mbcnt_hi(~0u, __builtin_amdgcn_mbcnt_lo(~0u, z)); }
;     const unsigned char* UV4 = (const unsigned char*)(F.ws + WS_UB) + (size_t)layer * (2u * TAB4);
;     const bf16* ZB = (const bf16*)(F.ws + WS_ZF); const bf16* PLE = (const bf16*)(F.ws + WS_PLE);
;     const int* IDX = (const int*)(F.ws + WS_IDX); const float* GWt = (const float*)(F.ws + WS_GW);
;     float* OF = (layer == 3 && !dummy) ? F.out : (float*)nullptr; bf16* XB = (bf16*)(F.ws + (dummy ? WS_X1B : WS_XB));
;     ...
;     const int idmask = (dummy == 1) ? PROBE_GATHER_MASK : 0x3fff;
;     ...
;     const float* gain1 = F.ln_gain + (size_t)(layer * 2) * D; const float* bias1 = F.ln_bias + (size_t)(layer * 2) * D;
;     const float* gain = F.ln_gain + (size_t)(layer * 2 + 1) * D; const float* bias = F.ln_bias + (size_t)(layer * 2 + 1) * D;
;     const int lane = fresh_lane();
;     const bool b3 = (lane & 8) != 0, b2 = (lane & 4) != 0, b1 = (lane & 2) != 0, b0 = (lane & 1) != 0;
;     const __amdgpu_buffer_rsrc_t rs = __builtin_amdgcn_make_buffer_rsrc((void*)UV4, (short)0, (int)(2u * TAB4), 0x00020000);
;     const unsigned voff = (unsigned)lane * 16u;
;     v4u ring[16];
;     int id0 = 0, id1 = 0, id0n = 0;
;     ...
;     int id1n = 0; float g0n = 0.f, g1n = 0.f;
;     if (F.gw < T) { gather_sorted_ids(IDX, GWt, F.gw, lane, id0n, id1n, g0n, g1n);
;     ...
;         id0n &= idmask; id1n &= idmask;
;     ...
; #pragma unroll
;         for (int k = 0; k < 16; ++k) GATHER_ISSUE(k, 256 + k); }
;     for (int t = F.gw; t < T; t += F.ngw) {
;         int xh[4], xl[4]; float xdq, mean1, rstd1;
;         {
;             const v4u hq = *(const v4u*)(F.ws + WS_XQ + (size_t)t * 2048 + lane * 32), lq = *(const v4u*)(F.ws + WS_XQ + (size_t)t * 2048 + lane * 32 + 16);
;             const f32x4 r4 = *(const f32x4*)(F.ws + WS_R4 + (size_t)t * 16);
;             xh[0] = (int)hq.x; xh[1] = (int)hq.y; xh[2] = (int)hq.z; xh[3] = (int)hq.w; xl[0] = (int)lq.x; xl[1] = (int)lq.y; xl[2] = (int)lq.z; xl[3] = (int)lq.w;
;             xdq = r4[0]; mean1 = r4[1]; rstd1 = r4[2];
;         }
;         if (t - F.wave + (NWAVES - 1) < T) __syncthreads();
;         id0 = id0n; id1 = id1n; const float g0 = g0n, g1 = g1n;
;         { const int tn = (t + F.ngw < T) ? t + F.ngw : t; gather_sorted_ids(IDX, GWt, tn, lane, id0n, id1n, g0n, g1n);
.LBB0_1412:
	s_andn2_b64 vcc, exec, s[14:15]
	s_cbranch_vccnz .LBB0_1452
	s_add_u32 s8, s60, 0x4a600000
	v_writelane_b32 v254, s8, 56
	s_addc_u32 s8, s61, 0
	v_writelane_b32 v255, s8, 5
	s_add_u32 s8, s60, 0x66600000
	v_writelane_b32 v255, s8, 7
	s_addc_u32 s8, s61, 0
	s_cmp_eq_u32 s18, 3
	v_writelane_b32 v255, s8, 9
	s_cselect_b64 s[8:9], -1, 0
	s_add_u32 s10, s60, 0x36600000
	v_writelane_b32 v255, s10, 11
	s_addc_u32 s43, s61, 0
	s_lshl_b32 s10, s18, 1
	s_mov_b64 s[16:17], s[80:81]
	v_writelane_b32 v255, s76, 1
	s_mov_b64 s[18:19], s[82:83]
	s_mov_b64 s[20:21], s[84:85]
	s_mov_b64 s[22:23], s[86:87]
	v_writelane_b32 v255, s77, 2
	v_readlane_b32 s76, v254, 1
	s_ashr_i32 s11, s10, 31
	v_readlane_b32 s90, v254, 15
	v_readlane_b32 s91, v254, 16
	s_lshl_b64 s[12:13], s[10:11], 13
	s_mov_b64 s[14:15], s[90:91]
	s_add_u32 s36, s14, s12
	s_addc_u32 s37, s15, s13
	s_add_u32 s12, s16, s12
	s_addc_u32 s13, s17, s13
	s_or_b32 s10, s10, 1
	v_readlane_b32 s72, v255, 1
	s_ashr_i32 s11, s10, 31
	v_readlane_b32 s73, v255, 2
	v_writelane_b32 v255, s12, 13
	s_lshl_b64 s[10:11], s[10:11], 13
	v_readlane_b32 s80, v254, 5
	v_writelane_b32 v255, s13, 14
	s_add_u32 s12, s14, s10
	s_addc_u32 s13, s15, s11
	v_readlane_b32 s81, v254, 6
	s_add_u32 s80, s16, s10
	s_addc_u32 s81, s17, s11
	v_readlane_b32 s10, v254, 51
	v_readlane_b32 s82, v254, 7
	v_readlane_b32 s83, v254, 8
	v_readlane_b32 s11, v254, 52
	s_and_b64 s[82:83], s[8:9], s[10:11]
	s_add_u32 s30, s60, 0x57600000
	v_writelane_b32 v255, s12, 15
	s_addc_u32 s39, s61, 0
	s_add_u32 s8, s60, 0x53200000
	v_writelane_b32 v255, s13, 16
	v_writelane_b32 v255, s8, 33
	s_addc_u32 s8, s61, 0
	v_writelane_b32 v255, s8, 35
	s_add_u32 s8, s60, 0x53600000
	v_writelane_b32 v255, s8, 29
	s_addc_u32 s8, s61, 0
	v_cmp_eq_u32_e64 s[28:29], 0, v68
	v_cmp_eq_u32_e32 vcc, 0, v67
	v_writelane_b32 v255, s8, 31
	s_xor_b64 s[44:45], vcc, s[28:29]
	v_cmp_eq_u32_e64 s[20:21], 0, v69
	v_writelane_b32 v255, s44, 17
	v_lshlrev_b32_e32 v70, 5, v130
	v_ashrrev_i32_e32 v71, 31, v70
	v_writelane_b32 v255, s45, 18
	s_xor_b64 s[44:45], vcc, s[20:21]
	v_writelane_b32 v255, s44, 19
	v_add_u32_e32 v194, 4, v66
	v_add_u32_e32 v195, 8, v66
	v_writelane_b32 v255, s45, 20
	s_xor_b64 s[44:45], vcc, s[0:1]
	v_writelane_b32 v255, s44, 21
	v_add_u32_e32 v196, 12, v66
	v_lshl_add_u64 v[66:67], s[60:61], 0, v[70:71]
	v_writelane_b32 v255, s45, 22
	s_xor_b64 s[44:45], vcc, s[2:3]
	v_writelane_b32 v255, s44, 23
	s_xor_b64 s[8:9], s[4:5], s[6:7]
	s_xor_b64 s[10:11], s[2:3], s[4:5]
	v_writelane_b32 v255, s45, 24
	s_xor_b64 s[44:45], vcc, s[4:5]
	v_writelane_b32 v255, s44, 25
	s_xor_b64 s[12:13], s[2:3], s[6:7]
	s_xor_b64 s[14:15], s[0:1], s[2:3]
	v_writelane_b32 v255, s45, 26
	s_xor_b64 s[44:45], vcc, s[6:7]
	v_writelane_b32 v255, s44, 27
	s_xor_b64 s[16:17], s[0:1], s[4:5]
	s_xor_b64 s[18:19], s[0:1], s[6:7]
	v_writelane_b32 v255, s45, 28
	s_mov_b64 s[44:45], 0x55600000
	s_xor_b64 s[22:23], s[20:21], s[0:1]
	s_xor_b64 s[24:25], s[20:21], s[2:3]
	s_xor_b64 s[26:27], s[20:21], s[4:5]
	v_ashrrev_i32_e32 v193, 4, v130
	v_lshl_add_u64 v[132:133], v[66:67], 0, s[44:45]
	s_xor_b64 s[44:45], s[20:21], s[6:7]
	s_xor_b64 s[46:47], s[28:29], s[20:21]
	s_xor_b64 s[48:49], s[28:29], s[0:1]
	s_xor_b64 s[50:51], s[28:29], s[2:3]
	s_xor_b64 s[52:53], s[28:29], s[4:5]
	s_xor_b64 s[54:55], s[28:29], s[6:7]
	v_readlane_b32 s77, v254, 2
	v_readlane_b32 s78, v254, 3
	v_readlane_b32 s79, v254, 4
	v_readlane_b32 s84, v254, 9
	v_readlane_b32 s85, v254, 10
	v_readlane_b32 s86, v254, 11
	v_readlane_b32 s87, v254, 12
	v_readlane_b32 s88, v254, 13
	v_readlane_b32 s89, v254, 14
	v_readlane_b32 s98, v254, 55
	s_lshl_b32 s98, s98, 6
	v_add_u32_e32 v228, s98, v130
	v_lshlrev_b32_e32 v228, 4, v228
	global_load_dwordx4 v[212:215], v228, s[36:37]
	global_load_dwordx4 v[224:227], v228, s[80:81]
	v_readlane_b32 s98, v255, 13
	v_readlane_b32 s99, v255, 14
	s_nop 4
	global_load_dwordx4 v[216:219], v228, s[98:99]
	v_readlane_b32 s98, v255, 15
	v_readlane_b32 s99, v255, 16
	s_nop 4
	global_load_dwordx4 v[220:223], v228, s[98:99]
	s_waitcnt vmcnt(3)
	ds_write_b128 v228, v[212:215]
	s_waitcnt vmcnt(2)
	ds_write_b128 v228, v[224:227] offset:24576
	s_waitcnt vmcnt(1)
	ds_write_b128 v228, v[216:219] offset:8192
	s_waitcnt vmcnt(0)
	ds_write_b128 v228, v[220:223] offset:16384
	s_waitcnt lgkmcnt(0)
	s_barrier
	v_readlane_b32 s100, v254, 58
	v_readlane_b32 s99, v255, 1
	s_add_i32 s99, s100, s99
	s_cmp_lt_i32 s99, 0x4000
	s_cselect_b32 s99, s99, s100
	s_lshl_b32 s100, s100, 12
	s_lshl_b32 s99, s99, 9
	v_lshl_add_u32 v244, v130, 6, s100
	v_lshl_add_u32 v249, v130, 2, s99
	v_readlane_b32 s100, v255, 7
	v_readlane_b32 s101, v255, 9
	s_nop 4
	global_load_dwordx4 v[212:215], v244, s[100:101] offset:48
	global_load_dwordx4 v[216:219], v244, s[100:101] offset:32
	global_load_dwordx4 v[220:223], v244, s[100:101] offset:16
	global_load_dwordx4 v[224:227], v244, s[100:101]
	v_readlane_b32 s100, v254, 56
	v_readlane_b32 s101, v255, 5
	s_nop 4
	global_load_dwordx4 v[228:231], v244, s[100:101] offset:48
	global_load_dwordx4 v[232:235], v244, s[100:101] offset:32
	global_load_dwordx4 v[236:239], v244, s[100:101] offset:16
	global_load_dwordx4 v[240:243], v244, s[100:101]
	global_load_dword v245, v249, s[70:71] offset:256
	global_load_dword v246, v249, s[40:41] offset:256
	global_load_dword v247, v249, s[40:41]
	global_load_dword v248, v249, s[70:71]
	v_readlane_b32 s98, v254, 55
	s_cmp_ge_u32 s98, 4
	s_cbranch_scc1 .Lprio_lo
	s_setprio 1
